# speedup vs baseline: 1.0005x; 1.0005x over previous
_Z9ln_kernelILi1ELi1EEvPKflS1_S1_S1_S1_S1_S1_S1_PfPDF16_S3_iii:
	s_load_dwordx4 s[8:11], s[0:1], 0x38
	s_load_dwordx4 s[16:19], s[0:1], 0x60
	s_load_dwordx2 s[20:21], s[0:1], 0x10
	s_load_dwordx4 s[12:15], s[0:1], 0x20
	s_bitcmp1_b32 s2, 8
	s_cbranch_scc0 .Lprio_skip_q1
	s_setprio 1
.Lprio_skip_q1:
	v_lshrrev_b32_e32 v1, 6, v0
	v_lshl_or_b32 v2, s2, 2, v1
	s_waitcnt lgkmcnt(0)
	s_cmp_gt_i32 s17, -1
	v_ashrrev_i32_e32 v3, 31, v2
	v_sub_u32_e32 v1, 0, v2
	s_cbranch_scc0 .LBB12_2
	s_abs_i32 s4, s16
	v_cvt_f32_u32_e32 v7, s4
	s_ashr_i32 s2, s18, 31
	v_mov_b32_e32 v4, s18
	v_mov_b32_e32 v5, s2
	v_rcp_iflag_f32_e32 v8, v7
	v_mad_u64_u32 v[4:5], s[2:3], s17, v2, v[4:5]
	v_mov_b32_e32 v6, v5
	v_mad_u64_u32 v[6:7], s[2:3], s17, v3, v[6:7]
	v_mul_f32_e32 v7, 0x4f7ffffe, v8
	v_cvt_u32_f32_e32 v7, v7
	s_sub_i32 s2, 0, s4
	v_max_i32_e32 v8, v2, v1
	v_mov_b32_e32 v5, v6
	v_mul_lo_u32 v9, s2, v7
	v_mul_hi_u32 v9, v7, v9
	v_add_u32_e32 v7, v7, v9
	v_mul_hi_u32 v7, v8, v7
	v_mul_lo_u32 v9, v7, s4
	v_sub_u32_e32 v8, v8, v9
	v_add_u32_e32 v9, 1, v7
	v_cmp_le_u32_e32 vcc, s4, v8
	v_xor_b32_e32 v6, s16, v2
	v_ashrrev_i32_e32 v6, 31, v6
	v_cndmask_b32_e32 v7, v7, v9, vcc
	v_subrev_u32_e32 v9, s4, v8
	v_cndmask_b32_e32 v8, v8, v9, vcc
	v_add_u32_e32 v9, 1, v7
	v_cmp_le_u32_e32 vcc, s4, v8
	s_mov_b64 s[26:27], 0
	s_nop 0
	v_cndmask_b32_e32 v7, v7, v9, vcc
	v_xor_b32_e32 v7, v7, v6
	v_sub_u32_e32 v6, v7, v6
	v_ashrrev_i32_e32 v7, 31, v6
	s_branch .LBB12_3

_Z9ln_kernelILi1ELi2EEvPKflS1_S1_S1_S1_S1_S1_S1_PfPDF16_S3_iii:
	s_load_dwordx4 s[8:11], s[0:1], 0x38
	s_load_dwordx4 s[16:19], s[0:1], 0x60
	s_load_dwordx2 s[20:21], s[0:1], 0x10
	s_load_dwordx4 s[12:15], s[0:1], 0x20
	s_bitcmp1_b32 s2, 8
	s_cbranch_scc0 .Lprio_skip_q2
	s_setprio 1

_Z9ln_kernelILi1ELi4EEvPKflS1_S1_S1_S1_S1_S1_S1_PfPDF16_S3_iii:
	s_load_dwordx4 s[8:11], s[0:1], 0x38
	s_load_dwordx4 s[16:19], s[0:1], 0x60
	s_load_dwordx2 s[20:21], s[0:1], 0x10
	s_load_dwordx4 s[12:15], s[0:1], 0x20
	s_bitcmp1_b32 s2, 8
	s_cbranch_scc0 .Lprio_skip_q3
	s_setprio 1
.Lprio_skip_q3:
	v_lshrrev_b32_e32 v1, 6, v0
	v_lshl_or_b32 v2, s2, 2, v1
	s_waitcnt lgkmcnt(0)
	s_cmp_gt_i32 s17, -1
	v_ashrrev_i32_e32 v3, 31, v2
	v_sub_u32_e32 v1, 0, v2
	s_cbranch_scc0 .LBB14_2
	s_abs_i32 s4, s16
	v_cvt_f32_u32_e32 v6, s4
	s_ashr_i32 s2, s18, 31
	v_mov_b32_e32 v4, s18
	v_mov_b32_e32 v5, s2
	v_rcp_iflag_f32_e32 v6, v6
	v_mad_u64_u32 v[8:9], s[2:3], s17, v2, v[4:5]
	v_mov_b32_e32 v4, v9
	v_mad_u64_u32 v[4:5], s[2:3], s17, v3, v[4:5]
	v_mul_f32_e32 v5, 0x4f7ffffe, v6
	v_cvt_u32_f32_e32 v5, v5
	s_sub_i32 s2, 0, s4
	v_max_i32_e32 v6, v2, v1
	v_mov_b32_e32 v9, v4
	v_mul_lo_u32 v7, s2, v5
	v_mul_hi_u32 v7, v5, v7
	v_add_u32_e32 v5, v5, v7
	v_mul_hi_u32 v5, v6, v5
	v_mul_lo_u32 v7, v5, s4
	v_sub_u32_e32 v6, v6, v7
	v_add_u32_e32 v7, 1, v5
	v_cmp_le_u32_e32 vcc, s4, v6
	v_xor_b32_e32 v4, s16, v2
	v_ashrrev_i32_e32 v4, 31, v4
	v_cndmask_b32_e32 v5, v5, v7, vcc
	v_subrev_u32_e32 v7, s4, v6
	v_cndmask_b32_e32 v6, v6, v7, vcc
	v_add_u32_e32 v7, 1, v5
	v_cmp_le_u32_e32 vcc, s4, v6
	s_mov_b64 s[26:27], 0
	s_nop 0
	v_cndmask_b32_e32 v5, v5, v7, vcc
	v_xor_b32_e32 v5, v5, v4
	v_sub_u32_e32 v6, v5, v4
	v_ashrrev_i32_e32 v7, 31, v6
	s_branch .LBB14_3

_Z9ln_kernelILi1ELi8EEvPKflS1_S1_S1_S1_S1_S1_S1_PfPDF16_S3_iii:
	s_load_dwordx4 s[8:11], s[0:1], 0x38
	s_load_dwordx4 s[16:19], s[0:1], 0x60
	s_load_dwordx2 s[20:21], s[0:1], 0x10
	s_load_dwordx4 s[12:15], s[0:1], 0x20
	s_bitcmp1_b32 s2, 8
	s_cbranch_scc0 .Lprio_skip_q4
	s_setprio 1

_Z6gemm_bILi2ELi4EEvPKDF16_S1_lS1_S1_iPKfPfllPDF16_S5_ifii:
	s_load_dword s4, s[0:1], 0x70
	s_load_dwordx2 s[10:11], s[0:1], 0x0
	s_load_dwordx2 s[8:9], s[0:1], 0x30
	s_bitcmp1_b32 s2, 8
	s_cbranch_scc0 .Lprio_skip_g24
	s_setprio 1
.Lprio_skip_g24:
	s_and_b32 s6, s2, 7
	s_waitcnt lgkmcnt(0)
	s_ashr_i32 s3, s4, 3
	s_and_b32 s4, s4, 7
	s_add_i32 s7, s3, 1
	s_cmp_ge_u32 s6, s4
	s_cbranch_scc0 .LBB16_2
	s_mul_i32 s5, s7, s4
	s_sub_i32 s4, s6, s4
	s_mul_i32 s4, s4, s3
	s_add_i32 s3, s5, s4
	s_load_dwordx2 s[12:13], s[0:1], 0x8
	s_cbranch_execz .LBB16_3
	s_branch .LBB16_4

_Z9ln_kernelILi0ELi1EEvPKflS1_S1_S1_S1_S1_S1_S1_PfPDF16_S3_iii:
	s_load_dwordx4 s[12:15], s[0:1], 0x60
	s_load_dwordx2 s[16:17], s[0:1], 0x10
	s_load_dwordx4 s[4:7], s[0:1], 0x20
	s_bitcmp1_b32 s2, 8
	s_cbranch_scc0 .Lprio_skip_q5
	s_setprio 1
.Lprio_skip_q5:
	v_lshrrev_b32_e32 v1, 6, v0
	v_lshl_or_b32 v6, s2, 2, v1
	s_waitcnt lgkmcnt(0)
	s_cmp_gt_i32 s13, -1
	v_ashrrev_i32_e32 v7, 31, v6
	s_cbranch_scc0 .LBB19_2
	s_ashr_i32 s2, s14, 31
	v_mov_b32_e32 v2, s14
	v_mov_b32_e32 v3, s2
	v_mad_u64_u32 v[2:3], s[2:3], s13, v6, v[2:3]
	v_mov_b32_e32 v4, v3
	v_mad_u64_u32 v[4:5], s[2:3], s13, v7, v[4:5]
	v_mov_b32_e32 v3, v4
	s_mov_b64 s[20:21], 0
	s_branch .LBB19_3

_Z9ln_kernelILi0ELi2EEvPKflS1_S1_S1_S1_S1_S1_S1_PfPDF16_S3_iii:
	s_load_dwordx4 s[12:15], s[0:1], 0x60
	s_load_dwordx2 s[16:17], s[0:1], 0x10
	s_load_dwordx4 s[8:11], s[0:1], 0x20
	s_bitcmp1_b32 s2, 8
	s_cbranch_scc0 .Lprio_skip_q6
	s_setprio 1
.Lprio_skip_q6:
	v_lshrrev_b32_e32 v1, 6, v0
	v_lshl_or_b32 v2, s2, 2, v1
	s_waitcnt lgkmcnt(0)
	s_cmp_gt_i32 s13, -1
	v_ashrrev_i32_e32 v3, 31, v2
	s_cbranch_scc0 .LBB20_2
	s_ashr_i32 s2, s14, 31
	v_mov_b32_e32 v4, s14
	v_mov_b32_e32 v5, s2
	v_mad_u64_u32 v[4:5], s[2:3], s13, v2, v[4:5]
	v_mov_b32_e32 v6, v5
	v_mad_u64_u32 v[6:7], s[2:3], s13, v3, v[6:7]
	v_mov_b32_e32 v5, v6
	s_mov_b64 s[20:21], 0
	s_branch .LBB20_3

_Z9ln_kernelILi0ELi4EEvPKflS1_S1_S1_S1_S1_S1_S1_PfPDF16_S3_iii:
	s_load_dwordx4 s[12:15], s[0:1], 0x60
	s_load_dwordx2 s[16:17], s[0:1], 0x10
	s_load_dwordx4 s[8:11], s[0:1], 0x20
	s_bitcmp1_b32 s2, 8
	s_cbranch_scc0 .Lprio_skip_q7
	s_setprio 1

_Z9ln_kernelILi0ELi8EEvPKflS1_S1_S1_S1_S1_S1_S1_PfPDF16_S3_iii:
	s_load_dwordx4 s[12:15], s[0:1], 0x60
	s_load_dwordx2 s[16:17], s[0:1], 0x10
	s_load_dwordx4 s[8:11], s[0:1], 0x20
	s_bitcmp1_b32 s2, 8
	s_cbranch_scc0 .Lprio_skip_q8
	s_setprio 1
